# speedup vs baseline: 1.0106x; 1.0106x over previous
.LBB3_8:
	s_or_b64 exec, exec, s[6:7]
	s_lshl_b32 s3, s2, 2
	s_and_b32 s26, s3, 28
	s_lshr_b32 s3, s2, 6
	s_lshl_b32 s2, s2, 1
	s_add_i32 s26, s26, s3
	s_and_b32 s22, s2, 64
	v_lshrrev_b32_e32 v47, 3, v0
	s_movk_i32 s2, 0x20f
	s_lshl_b32 s23, s26, 2
	v_mov_b32_e32 v4, 0xffffffbe
	v_cmp_lt_u32_e64 s[6:7], s2, v0
	v_or_b32_e32 v66, 64, v47
	v_mul_lo_u16_e32 v6, 63, v66
	v_cndmask_b32_e64 v70, 0, v4, s[6:7]
	v_mov_b32_e32 v4, s23
	s_add_i32 s25, s23, -1
	s_add_i32 s27, s22, -1
	v_lshlrev_b32_e32 v28, 3, v0
	v_addc_co_u32_e64 v71, vcc, -1, v4, s[6:7]
	v_mov_b32_e32 v8, 0x7f
	v_lshrrev_b16_e32 v65, 12, v6
	v_and_b32_e32 v30, 56, v28
	v_med3_i32 v4, v71, 0, v8
	v_add3_u32 v5, s27, v47, v70
	v_mul_i32_i24_e32 v68, 0xffffffbe, v65
	v_add_u32_e32 v67, s25, v65
	v_lshlrev_b32_e32 v26, 1, v30
	v_mov_b32_e32 v27, 0
	v_med3_i32 v5, v5, 0, v8
	v_lshlrev_b32_e32 v4, 14, v4
	v_med3_i32 v6, v67, 0, v8
	v_add3_u32 v7, s27, v66, v68
	s_waitcnt lgkmcnt(0)
	v_lshl_add_u64 v[2:3], s[12:13], 0, v[26:27]
	v_lshl_or_b32 v26, v5, 7, v4
	v_med3_i32 v7, v7, 0, v8
	v_lshlrev_b32_e32 v6, 14, v6
	v_lshl_add_u64 v[4:5], v[2:3], 0, v[26:27]
	v_lshl_or_b32 v26, v7, 7, v6
	v_or_b32_e32 v62, 0x80, v47
	v_lshl_add_u64 v[6:7], v[2:3], 0, v[26:27]
	global_load_dwordx4 v[42:45], v[4:5], off
	global_load_dwordx4 v[22:25], v[6:7], off
	v_mul_lo_u16_e32 v4, 0xf9, v62
	v_or_b32_e32 v58, 0xc0, v47
	v_lshrrev_b16_e32 v61, 14, v4
	v_mul_u32_u24_e32 v6, 0x3e1, v58
	v_mul_i32_i24_e32 v64, 0xffffffbe, v61
	v_add_u32_e32 v63, s25, v61
	v_lshrrev_b32_e32 v57, 16, v6
	v_min_u32_e32 v4, 0x7f, v63
	v_add3_u32 v5, s27, v62, v64
	v_mul_i32_i24_e32 v60, 0xffffffbe, v57
	v_add_u32_e32 v59, s25, v57
	v_med3_i32 v5, v5, 0, v8
	v_lshlrev_b32_e32 v4, 14, v4
	v_min_u32_e32 v6, 0x7f, v59
	v_add3_u32 v7, s27, v58, v60
	v_lshl_or_b32 v26, v5, 7, v4
	v_med3_i32 v7, v7, 0, v8
	v_lshlrev_b32_e32 v6, 14, v6
	v_lshl_add_u64 v[4:5], v[2:3], 0, v[26:27]
	v_lshl_or_b32 v26, v7, 7, v6
	v_or_b32_e32 v54, 0x100, v47
	v_lshl_add_u64 v[6:7], v[2:3], 0, v[26:27]
	global_load_dwordx4 v[18:21], v[4:5], off
	global_load_dwordx4 v[14:17], v[6:7], off
	v_mul_u32_u24_e32 v4, 0x3e1, v54
	v_lshrrev_b32_e32 v53, 16, v4
	v_or_b32_e32 v52, 0x140, v47
	s_movk_i32 s3, 0xffbe
	v_mul_i32_i24_e32 v56, 0xffffffbe, v53
	v_add_u32_e32 v55, s25, v53
	v_mul_u32_u24_e32 v6, 0x3e1, v52
	v_min_u32_e32 v4, 0x7f, v55
	v_add3_u32 v5, s27, v54, v56
	v_mul_i32_i24_sdwa v7, v6, s3 dst_sel:DWORD dst_unused:UNUSED_PAD src0_sel:WORD_1 src1_sel:DWORD
	v_add_u32_sdwa v6, s25, v6 dst_sel:DWORD dst_unused:UNUSED_PAD src0_sel:DWORD src1_sel:WORD_1
	v_med3_i32 v5, v5, 0, v8
	v_lshlrev_b32_e32 v4, 14, v4
	v_min_u32_e32 v6, 0x7f, v6
	v_add3_u32 v7, s27, v52, v7
	v_lshl_or_b32 v26, v5, 7, v4
	v_med3_i32 v7, v7, 0, v8
	v_lshlrev_b32_e32 v6, 14, v6
	v_lshl_add_u64 v[4:5], v[2:3], 0, v[26:27]
	v_lshl_or_b32 v26, v7, 7, v6
	v_or_b32_e32 v51, 0x180, v47
	v_lshl_add_u64 v[32:33], v[2:3], 0, v[26:27]
	global_load_dwordx4 v[10:13], v[4:5], off
	global_load_dwordx4 v[6:9], v[32:33], off
	v_min_u32_e32 v4, 0x18b, v51
	s_min_u32 s2, s23, 0x7b
	v_add_u32_e32 v4, s27, v4
	v_add_u32_e32 v4, 0xfffffeb6, v4
	s_lshl_b32 s2, s2, 14
	v_min_u32_e32 v4, 0x7f, v4
	s_add_i32 s2, s2, 0x10000
	v_lshl_or_b32 v26, v4, 7, s2
	v_lshl_add_u64 v[2:3], v[2:3], 0, v[26:27]
	global_load_dwordx4 v[2:5], v[2:3], off
	s_load_dwordx4 s[16:19], s[0:1], 0x10
	v_and_b32_e32 v28, 63, v0
	v_lshlrev_b32_e32 v28, 4, v28
	global_load_dwordx4 v[36:39], v28, s[14:15]
	global_load_dwordx4 v[32:35], v28, s[14:15] offset:1024
	v_lshlrev_b32_e32 v28, 2, v30
	s_waitcnt lgkmcnt(0)
	global_load_dwordx4 v[76:79], v28, s[16:17]
	global_load_dwordx4 v[80:83], v28, s[16:17] offset:16
	global_load_dwordx4 v[84:87], v28, s[18:19]
	global_load_dwordx4 v[176:179], v28, s[18:19] offset:16
	s_movk_i32 s38, 0xff94
	s_movk_i32 s39, 0xffee
	s_add_i32 s40, s22, -4
	v_mov_b32_e32 v131, 0x7f
	v_mov_b32_e32 v132, 0x7c
	v_min_u32_e32 v133, 27, v50
	v_min_u32_e32 v134, 3, v48
	v_or_b32_e32 v134, 24, v134
	v_lshl_or_b32 v128, v48, 6, v1
	v_mul_u32_u24_e32 v129, 0x25f, v128
	v_lshrrev_b32_e32 v129, 16, v129
	v_mad_i32_i24 v128, v129, s38, v128
	v_mul_u32_u24_e32 v130, 0xe39, v128
	v_lshrrev_b32_e32 v130, 16, v130
	v_mad_i32_i24 v128, v130, s39, v128
	v_add_u32_e32 v130, s25, v130
	v_med3_i32 v130, v130, 0, v131
	v_lshl_add_u32 v128, v128, 2, s40
	v_med3_i32 v128, v128, 0, v132
	v_min_u32_e32 v129, 15, v129
	v_lshlrev_b32_e32 v129, 14, v129
	v_lshlrev_b32_e32 v130, 7, v130
	v_or3_b32 v94, v130, v129, v128
	v_lshl_or_b32 v128, v49, 6, v1
	v_mul_u32_u24_e32 v129, 0x25f, v128
	v_lshrrev_b32_e32 v129, 16, v129
	v_mad_i32_i24 v128, v129, s38, v128
	v_mul_u32_u24_e32 v130, 0xe39, v128
	v_lshrrev_b32_e32 v130, 16, v130
	v_mad_i32_i24 v128, v130, s39, v128
	v_add_u32_e32 v130, s25, v130
	v_med3_i32 v130, v130, 0, v131
	v_lshl_add_u32 v128, v128, 2, s40
	v_med3_i32 v128, v128, 0, v132
	v_min_u32_e32 v129, 15, v129
	v_lshlrev_b32_e32 v129, 14, v129
	v_lshlrev_b32_e32 v130, 7, v130
	v_or3_b32 v96, v130, v129, v128
	v_lshl_or_b32 v128, v133, 6, v1
	v_mul_u32_u24_e32 v129, 0x25f, v128
	v_lshrrev_b32_e32 v129, 16, v129
	v_mad_i32_i24 v128, v129, s38, v128
	v_mul_u32_u24_e32 v130, 0xe39, v128
	v_lshrrev_b32_e32 v130, 16, v130
	v_mad_i32_i24 v128, v130, s39, v128
	v_add_u32_e32 v130, s25, v130
	v_med3_i32 v130, v130, 0, v131
	v_lshl_add_u32 v128, v128, 2, s40
	v_med3_i32 v128, v128, 0, v132
	v_min_u32_e32 v129, 15, v129
	v_lshlrev_b32_e32 v129, 14, v129
	v_lshlrev_b32_e32 v130, 7, v130
	v_or3_b32 v98, v130, v129, v128
	v_lshl_or_b32 v128, v134, 6, v1
	v_mul_u32_u24_e32 v129, 0x25f, v128
	v_lshrrev_b32_e32 v129, 16, v129
	v_mad_i32_i24 v128, v129, s38, v128
	v_mul_u32_u24_e32 v130, 0xe39, v128
	v_lshrrev_b32_e32 v130, 16, v130
	v_mad_i32_i24 v128, v130, s39, v128
	v_add_u32_e32 v130, s25, v130
	v_med3_i32 v130, v130, 0, v131
	v_lshl_add_u32 v128, v128, 2, s40
	v_med3_i32 v128, v128, 0, v132
	v_min_u32_e32 v129, 15, v129
	v_lshlrev_b32_e32 v129, 14, v129
	v_lshlrev_b32_e32 v130, 7, v130
	v_or3_b32 v100, v130, v129, v128
	v_cmp_eq_u32_e32 vcc, 27, v134
	v_readfirstlane_b32 s41, v100
	s_nop 1
	v_mov_b32_e32 v135, s41
	v_cndmask_b32_e32 v100, v100, v135, vcc
	v_accvgpr_write_b32 a3, 0
	v_accvgpr_write_b32 a2, 0
	v_accvgpr_write_b32 a1, 0
	v_accvgpr_write_b32 a0, 0
	v_accvgpr_write_b32 a7, 0
	v_accvgpr_write_b32 a6, 0
	v_accvgpr_write_b32 a5, 0
	v_accvgpr_write_b32 a4, 0
	v_accvgpr_write_b32 a15, 0
	v_accvgpr_write_b32 a14, 0
	v_accvgpr_write_b32 a13, 0
	v_accvgpr_write_b32 a12, 0
	v_accvgpr_write_b32 a19, 0
	v_accvgpr_write_b32 a18, 0
	v_accvgpr_write_b32 a17, 0
	v_accvgpr_write_b32 a16, 0
	v_accvgpr_write_b32 a31, 0
	v_accvgpr_write_b32 a30, 0
	v_accvgpr_write_b32 a29, 0
	v_accvgpr_write_b32 a28, 0
	v_accvgpr_write_b32 a63, 0
	v_accvgpr_write_b32 a62, 0
	v_accvgpr_write_b32 a61, 0
	v_accvgpr_write_b32 a60, 0
	v_accvgpr_write_b32 a11, 0
	v_accvgpr_write_b32 a10, 0
	v_accvgpr_write_b32 a9, 0
	v_accvgpr_write_b32 a8, 0
	v_accvgpr_write_b32 a23, 0
	v_accvgpr_write_b32 a22, 0
	v_accvgpr_write_b32 a21, 0
	v_accvgpr_write_b32 a20, 0
	v_accvgpr_write_b32 a27, 0
	v_accvgpr_write_b32 a26, 0
	v_accvgpr_write_b32 a25, 0
	v_accvgpr_write_b32 a24, 0
	v_accvgpr_write_b32 a39, 0
	v_accvgpr_write_b32 a38, 0
	v_accvgpr_write_b32 a37, 0
	v_accvgpr_write_b32 a36, 0
	v_accvgpr_write_b32 a47, 0
	v_accvgpr_write_b32 a46, 0
	v_accvgpr_write_b32 a45, 0
	v_accvgpr_write_b32 a44, 0
	v_accvgpr_write_b32 a67, 0
	v_accvgpr_write_b32 a66, 0
	v_accvgpr_write_b32 a65, 0
	v_accvgpr_write_b32 a64, 0
	v_accvgpr_write_b32 a35, 0
	v_accvgpr_write_b32 a34, 0
	v_accvgpr_write_b32 a33, 0
	v_accvgpr_write_b32 a32, 0
	v_accvgpr_write_b32 a43, 0
	v_accvgpr_write_b32 a42, 0
	v_accvgpr_write_b32 a41, 0
	v_accvgpr_write_b32 a40, 0
	v_accvgpr_write_b32 a51, 0
	v_accvgpr_write_b32 a50, 0
	v_accvgpr_write_b32 a49, 0
	v_accvgpr_write_b32 a48, 0
	v_accvgpr_write_b32 a55, 0
	v_accvgpr_write_b32 a54, 0
	v_accvgpr_write_b32 a53, 0
	v_accvgpr_write_b32 a52, 0
	v_accvgpr_write_b32 a59, 0
	v_accvgpr_write_b32 a58, 0
	v_accvgpr_write_b32 a57, 0
	v_accvgpr_write_b32 a56, 0
	v_accvgpr_write_b32 a71, 0
	v_accvgpr_write_b32 a70, 0
	v_accvgpr_write_b32 a69, 0
	v_accvgpr_write_b32 a68, 0
	v_readfirstlane_b32 s42, v118
	v_and_b32_e32 v130, 63, v0
	v_lshlrev_b32_e32 v130, 4, v130
	v_bfe_u32 v131, v0, 6, 2
	v_bfe_u32 v132, v0, 4, 2
	v_lshrrev_b32_e32 v133, 8, v0
	v_and_b32_e32 v129, 15, v0
	v_lshl_or_b32 v133, v133, 4, v129
	s_add_i32 s43, s42, 0x2000
	s_add_i32 s44, s42, 0x4000
	v_add_u32_e32 v137, s42, v130
	v_add_u32_e32 v138, 0x2000, v137
	v_add_u32_e32 v139, 0x4000, v137
	v_add_u32_e32 v164, 0xc600, v130
	v_add_u32_e32 v165, 0x10e00, v130
	v_add_u32_e32 v166, 0x16000, v130
	v_add_u32_e32 v167, 0x1a800, v130
	v_add_u32_e32 v168, 0x1f000, v130
	s_add_u32 s52, s50, 0x9000
	s_addc_u32 s53, s51, 0
	s_add_i32 m0, s42, 0x16000
	s_nop 0
	global_load_lds_dwordx4 v137, s[52:53]
	s_add_i32 m0, s43, 0x16000
	s_nop 0
	global_load_lds_dwordx4 v138, s[52:53]
	s_cmp_lt_u32 s42, 0x800
	s_cbranch_scc0 .Lk4_sp2
	s_add_i32 m0, s44, 0x16000
	s_nop 0
	global_load_lds_dwordx4 v139, s[52:53]

.Lk4_sp4:
	v_lshl_add_u32 v128, v131, 1, 0
	v_lshl_add_u32 v128, v128, 5, v128
	v_add3_u32 v128, v128, v133, 0
	v_bitop3_b32 v129, v128, v132, 7 bitop3:0x6c
	v_lshlrev_b32_e32 v128, 7, v128
	v_lshl_or_b32 v140, v129, 4, v128
	v_xor_b32_e32 v141, 64, v140
	v_lshl_add_u32 v128, v131, 1, 1
	v_lshl_add_u32 v128, v128, 5, v128
	v_add3_u32 v128, v128, v133, 0
	v_bitop3_b32 v129, v128, v132, 7 bitop3:0x6c
	v_lshlrev_b32_e32 v128, 7, v128
	v_lshl_or_b32 v142, v129, 4, v128
	v_xor_b32_e32 v143, 64, v142
	v_lshl_add_u32 v128, v131, 1, 0
	v_lshl_add_u32 v128, v128, 5, v128
	v_add3_u32 v128, v128, v133, 1
	v_bitop3_b32 v129, v128, v132, 7 bitop3:0x6c
	v_lshlrev_b32_e32 v128, 7, v128
	v_lshl_or_b32 v144, v129, 4, v128
	v_xor_b32_e32 v145, 64, v144
	v_lshl_add_u32 v128, v131, 1, 1
	v_lshl_add_u32 v128, v128, 5, v128
	v_add3_u32 v128, v128, v133, 1
	v_bitop3_b32 v129, v128, v132, 7 bitop3:0x6c
	v_lshlrev_b32_e32 v128, 7, v128
	v_lshl_or_b32 v146, v129, 4, v128
	v_xor_b32_e32 v147, 64, v146
	v_lshl_add_u32 v128, v131, 1, 2
	v_lshl_add_u32 v128, v128, 5, v128
	v_add3_u32 v128, v128, v133, 0
	v_bitop3_b32 v129, v128, v132, 7 bitop3:0x6c
	v_lshlrev_b32_e32 v128, 7, v128
	v_lshl_or_b32 v148, v129, 4, v128
	v_xor_b32_e32 v149, 64, v148
	v_lshl_add_u32 v128, v131, 1, 3
	v_lshl_add_u32 v128, v128, 5, v128
	v_add3_u32 v128, v128, v133, 0
	v_bitop3_b32 v129, v128, v132, 7 bitop3:0x6c
	v_lshlrev_b32_e32 v128, 7, v128
	v_lshl_or_b32 v150, v129, 4, v128
	v_xor_b32_e32 v151, 64, v150
	v_lshl_add_u32 v128, v131, 1, 2
	v_lshl_add_u32 v128, v128, 5, v128
	v_add3_u32 v128, v128, v133, 1
	v_bitop3_b32 v129, v128, v132, 7 bitop3:0x6c
	v_lshlrev_b32_e32 v128, 7, v128
	v_lshl_or_b32 v152, v129, 4, v128
	v_xor_b32_e32 v153, 64, v152
	v_lshl_add_u32 v128, v131, 1, 3
	v_lshl_add_u32 v128, v128, 5, v128
	v_add3_u32 v128, v128, v133, 1
	v_bitop3_b32 v129, v128, v132, 7 bitop3:0x6c
	v_lshlrev_b32_e32 v128, 7, v128
	v_lshl_or_b32 v154, v129, 4, v128
	v_xor_b32_e32 v155, 64, v154
	v_lshl_add_u32 v128, v131, 1, 4
	v_lshl_add_u32 v128, v128, 5, v128
	v_add3_u32 v128, v128, v133, 0
	v_bitop3_b32 v129, v128, v132, 7 bitop3:0x6c
	v_lshlrev_b32_e32 v128, 7, v128
	v_lshl_or_b32 v156, v129, 4, v128
	v_xor_b32_e32 v157, 64, v156
	v_lshl_add_u32 v128, v131, 1, 5
	v_lshl_add_u32 v128, v128, 5, v128
	v_add3_u32 v128, v128, v133, 0
	v_bitop3_b32 v129, v128, v132, 7 bitop3:0x6c
	v_lshlrev_b32_e32 v128, 7, v128
	v_lshl_or_b32 v158, v129, 4, v128
	v_xor_b32_e32 v159, 64, v158
	v_lshl_add_u32 v128, v131, 1, 4
	v_lshl_add_u32 v128, v128, 5, v128
	v_add3_u32 v128, v128, v133, 1
	v_bitop3_b32 v129, v128, v132, 7 bitop3:0x6c
	v_lshlrev_b32_e32 v128, 7, v128
	v_lshl_or_b32 v160, v129, 4, v128
	v_xor_b32_e32 v161, 64, v160
	v_lshl_add_u32 v128, v131, 1, 5
	v_lshl_add_u32 v128, v128, 5, v128
	v_add3_u32 v128, v128, v133, 1
	v_bitop3_b32 v129, v128, v132, 7 bitop3:0x6c
	v_lshlrev_b32_e32 v128, 7, v128
	v_lshl_or_b32 v162, v129, 4, v128
	v_xor_b32_e32 v163, 64, v162
	s_waitcnt vmcnt(6)
	v_pk_add_f32 v[36:37], v[36:37], v[38:39]
	v_pk_add_f32 v[32:33], v[32:33], v[34:35]
	v_pk_add_f32 v[26:27], v[36:37], v[32:33]
	s_nop 1
	v_mov_b32_dpp v28, v26 row_shr:1 row_mask:0xf bank_mask:0xf bound_ctrl:1
	v_mov_b32_dpp v29, v27 row_shr:1 row_mask:0xf bank_mask:0xf bound_ctrl:1
	v_pk_add_f32 v[26:27], v[26:27], v[28:29]
	v_mov_b32_e32 v34, 0
	v_mov_b32_e32 v35, 0
	v_mov_b32_dpp v28, v26 row_shr:2 row_mask:0xf bank_mask:0xf bound_ctrl:1
	v_mov_b32_dpp v29, v27 row_shr:2 row_mask:0xf bank_mask:0xf bound_ctrl:1
	v_pk_add_f32 v[26:27], v[26:27], v[28:29]
	v_cmp_eq_u32_e32 vcc, 63, v1
	s_nop 0
	v_mov_b32_dpp v28, v26 row_shr:4 row_mask:0xf bank_mask:0xf bound_ctrl:1
	v_mov_b32_dpp v29, v27 row_shr:4 row_mask:0xf bank_mask:0xf bound_ctrl:1
	v_pk_add_f32 v[26:27], v[26:27], v[28:29]
	s_nop 1
	v_mov_b32_dpp v28, v26 row_shr:8 row_mask:0xf bank_mask:0xf bound_ctrl:1
	v_mov_b32_dpp v29, v27 row_shr:8 row_mask:0xf bank_mask:0xf bound_ctrl:1
	v_pk_add_f32 v[28:29], v[26:27], v[28:29]
	v_mov_b32_e32 v27, 0
	v_mov_b32_e32 v26, 0
	v_mov_b32_dpp v34, v28 row_bcast:15 row_mask:0xa bank_mask:0xf
	v_mov_b32_dpp v35, v29 row_bcast:15 row_mask:0xa bank_mask:0xf
	v_pk_add_f32 v[28:29], v[28:29], v[34:35]
	s_nop 1
	v_mov_b32_dpp v26, v28 row_bcast:31 row_mask:0xc bank_mask:0xf
	v_mov_b32_dpp v27, v29 row_bcast:31 row_mask:0xc bank_mask:0xf
	v_pk_add_f32 v[26:27], v[28:29], v[26:27]
	s_mov_b32 s2, 0xf800000
	s_nop 0
	v_readlane_b32 s46, v26, 63
	v_readlane_b32 s47, v27, 63
	s_nop 3
	v_mov_b32_e32 v26, s46
	v_mov_b32_e32 v27, s47
	v_mul_f32_e32 v26, 0x35800000, v26
	v_mul_f32_e32 v27, 0x35800000, v27
	v_fma_f32 v27, -v26, v26, v27
	v_add_f32_e32 v27, 0x3727c5ac, v27
	v_mul_f32_e32 v28, 0x4f800000, v27
	v_cmp_gt_f32_e32 vcc, s2, v27
	s_nop 1
	v_cndmask_b32_e32 v27, v27, v28, vcc
	v_sqrt_f32_e32 v28, v27
	s_nop 0
	v_add_u32_e32 v29, -1, v28
	v_fma_f32 v33, -v29, v28, v27
	v_cmp_ge_f32_e64 s[2:3], 0, v33
	v_add_u32_e32 v33, 1, v28
	s_nop 0
	v_cndmask_b32_e64 v29, v28, v29, s[2:3]
	v_fma_f32 v28, -v33, v28, v27
	v_cmp_lt_f32_e64 s[2:3], 0, v28
	s_nop 1
	v_cndmask_b32_e64 v28, v29, v33, s[2:3]
	v_mul_f32_e32 v29, 0x37800000, v28
	v_cndmask_b32_e32 v28, v28, v29, vcc
	v_mov_b32_e32 v29, 0x260
	v_cmp_class_f32_e32 vcc, v27, v29
	s_nop 1
	v_cndmask_b32_e32 v27, v28, v27, vcc
	v_div_scale_f32 v28, s[2:3], v27, v27, 1.0
	v_rcp_f32_e32 v29, v28
	s_nop 0
	v_fma_f32 v33, -v28, v29, 1.0
	v_fmac_f32_e32 v29, v33, v29
	v_div_scale_f32 v33, vcc, 1.0, v27, 1.0
	v_mul_f32_e32 v34, v33, v29
	v_fma_f32 v35, -v28, v34, v33
	v_fmac_f32_e32 v34, v35, v29
	v_fma_f32 v28, -v28, v34, v33
	v_div_fmas_f32 v28, v28, v29, v34
	v_div_fixup_f32 v27, v28, v27, 1.0
	v_mov_b32_e32 v169, v26
	v_mov_b32_e32 v170, v27
	v_mul_f32_e32 v26, v76, v170
	v_mul_f32_e32 v27, v77, v170
	v_mul_f32_e32 v28, v78, v170
	v_mul_f32_e32 v29, v79, v170
	v_mul_f32_e32 v34, v80, v170
	v_mul_f32_e32 v35, v81, v170
	v_mul_f32_e32 v36, v82, v170
	v_mul_f32_e32 v37, v83, v170
	v_fma_f32 v30, -v169, v26, v84
	v_fma_f32 v31, -v169, v27, v85
	v_fma_f32 v32, -v169, v28, v86
	v_fma_f32 v33, -v169, v29, v87
	v_fma_f32 v38, -v169, v34, v176
	v_fma_f32 v39, -v169, v35, v177
	v_fma_f32 v40, -v169, v36, v178
	v_fma_f32 v41, -v169, v37, v179
	v_fma_mixlo_f16 v72, v42, v26, v30 op_sel_hi:[1,0,0]
	v_fma_mixhi_f16 v72, v42, v27, v31 op_sel:[1,0,0] op_sel_hi:[1,0,0]
	v_pk_max_f16 v72, v72, 0
	v_add3_u32 v42, v70, v47, s27
	v_add_u16_e32 v70, v70, v47
	v_bfe_u32 v69, v0, 3, 1
	v_max_u32_e32 v42, v71, v42
	v_cndmask_b32_e64 v71, 0, 2, s[6:7]
	v_ashrrev_i16_e32 v70, 1, v70
	v_or_b32_e32 v71, v71, v69
	v_bfe_i32 v70, v70, 0, 16
	v_mad_u32_u24 v70, v71, 33, v70
	v_lshlrev_b32_e32 v71, 7, v70
	v_xor_b32_e32 v70, v70, v0
	s_movk_i32 s10, 0x80
	v_lshlrev_b32_e32 v70, 4, v70
	v_cmp_gt_u32_e32 vcc, s10, v42
	v_and_b32_e32 v70, 0x70, v70
	v_fma_mixlo_f16 v73, v43, v28, v32 op_sel_hi:[1,0,0]
	v_fma_mixhi_f16 v73, v43, v29, v33 op_sel:[1,0,0] op_sel_hi:[1,0,0]
	v_pk_max_f16 v73, v73, 0
	s_waitcnt lgkmcnt(0)
	v_fma_mixlo_f16 v74, v44, v34, v38 op_sel_hi:[1,0,0]
	v_fma_mixhi_f16 v74, v44, v35, v39 op_sel:[1,0,0] op_sel_hi:[1,0,0]
	v_pk_max_f16 v74, v74, 0
	v_fma_mixlo_f16 v75, v45, v36, v40 op_sel_hi:[1,0,0]
	v_fma_mixhi_f16 v75, v45, v37, v41 op_sel:[1,0,0] op_sel_hi:[1,0,0]
	v_pk_max_f16 v75, v75, 0
	v_add3_u32 v70, 0, v71, v70
	v_cndmask_b32_e32 v42, 0, v72, vcc
	v_cndmask_b32_e32 v43, 0, v73, vcc
	v_cndmask_b32_e32 v44, 0, v74, vcc
	v_cndmask_b32_e32 v45, 0, v75, vcc
	v_add_u32_e32 v66, v68, v66
	ds_write_b128 v70, v[42:45]
	v_fma_mixlo_f16 v42, v22, v26, v30 op_sel_hi:[1,0,0]
	v_fma_mixhi_f16 v42, v22, v27, v31 op_sel:[1,0,0] op_sel_hi:[1,0,0]
	v_pk_max_f16 v42, v42, 0
	v_add_u32_e32 v22, s27, v66
	v_max_u32_e32 v22, v67, v22
	v_fma_mixlo_f16 v43, v23, v28, v32 op_sel_hi:[1,0,0]
	v_fma_mixhi_f16 v43, v23, v29, v33 op_sel:[1,0,0] op_sel_hi:[1,0,0]
	v_pk_max_f16 v43, v43, 0
	v_cmp_gt_u32_e32 vcc, s10, v22
	v_fma_mixlo_f16 v44, v24, v34, v38 op_sel_hi:[1,0,0]
	v_fma_mixhi_f16 v44, v24, v35, v39 op_sel:[1,0,0] op_sel_hi:[1,0,0]
	v_pk_max_f16 v44, v44, 0
	v_fma_mixlo_f16 v45, v25, v36, v40 op_sel_hi:[1,0,0]
	v_fma_mixhi_f16 v45, v25, v37, v41 op_sel:[1,0,0] op_sel_hi:[1,0,0]
	v_pk_max_f16 v45, v45, 0
	s_load_dwordx2 s[2:3], s[0:1], 0x28
	s_movk_i32 s6, 0x260
	v_cndmask_b32_e32 v22, 0, v42, vcc
	v_cndmask_b32_e32 v23, 0, v43, vcc
	v_lshl_or_b32 v42, v65, 1, v69
	v_ashrrev_i32_e32 v43, 1, v66
	v_mad_u32_u24 v42, v42, 33, v43
	v_lshlrev_b32_e32 v43, 7, v42
	v_xor_b32_e32 v42, v42, v0
	v_lshlrev_b32_e32 v42, 4, v42
	v_and_b32_e32 v42, 0x70, v42
	v_cndmask_b32_e32 v24, 0, v44, vcc
	v_cndmask_b32_e32 v25, 0, v45, vcc
	v_add3_u32 v42, 0, v43, v42
	ds_write_b128 v42, v[22:25]
	v_add_u32_e32 v42, v64, v62
	v_fma_mixlo_f16 v22, v18, v26, v30 op_sel_hi:[1,0,0]
	v_fma_mixhi_f16 v22, v18, v27, v31 op_sel:[1,0,0] op_sel_hi:[1,0,0]
	v_pk_max_f16 v22, v22, 0
	v_add_u32_e32 v18, s27, v42
	v_max_u32_e32 v18, v63, v18
	v_fma_mixlo_f16 v23, v19, v28, v32 op_sel_hi:[1,0,0]
	v_fma_mixhi_f16 v23, v19, v29, v33 op_sel:[1,0,0] op_sel_hi:[1,0,0]
	v_pk_max_f16 v23, v23, 0
	v_cmp_gt_u32_e32 vcc, s10, v18
	v_fma_mixlo_f16 v24, v20, v34, v38 op_sel_hi:[1,0,0]
	v_fma_mixhi_f16 v24, v20, v35, v39 op_sel:[1,0,0] op_sel_hi:[1,0,0]
	v_pk_max_f16 v24, v24, 0
	v_fma_mixlo_f16 v25, v21, v36, v40 op_sel_hi:[1,0,0]
	v_fma_mixhi_f16 v25, v21, v37, v41 op_sel:[1,0,0] op_sel_hi:[1,0,0]
	v_pk_max_f16 v25, v25, 0
	s_nop 1
	v_cndmask_b32_e32 v18, 0, v22, vcc
	v_cndmask_b32_e32 v19, 0, v23, vcc
	v_lshl_or_b32 v22, v61, 1, v69
	v_ashrrev_i32_e32 v23, 1, v42
	v_mad_u32_u24 v22, v22, 33, v23
	v_lshlrev_b32_e32 v23, 7, v22
	v_xor_b32_e32 v22, v22, v0
	v_lshlrev_b32_e32 v22, 4, v22
	v_and_b32_e32 v22, 0x70, v22
	v_cndmask_b32_e32 v20, 0, v24, vcc
	v_cndmask_b32_e32 v21, 0, v25, vcc
	v_add3_u32 v22, 0, v23, v22
	ds_write_b128 v22, v[18:21]
	v_add_u32_e32 v22, v60, v58
	v_fma_mixlo_f16 v18, v14, v26, v30 op_sel_hi:[1,0,0]
	v_fma_mixhi_f16 v18, v14, v27, v31 op_sel:[1,0,0] op_sel_hi:[1,0,0]
	v_pk_max_f16 v18, v18, 0
	v_add_u32_e32 v14, s27, v22
	v_max_u32_e32 v14, v59, v14
	v_fma_mixlo_f16 v19, v15, v28, v32 op_sel_hi:[1,0,0]
	v_fma_mixhi_f16 v19, v15, v29, v33 op_sel:[1,0,0] op_sel_hi:[1,0,0]
	v_pk_max_f16 v19, v19, 0
	v_cmp_gt_u32_e32 vcc, s10, v14
	v_fma_mixlo_f16 v20, v16, v34, v38 op_sel_hi:[1,0,0]
	v_fma_mixhi_f16 v20, v16, v35, v39 op_sel:[1,0,0] op_sel_hi:[1,0,0]
	v_pk_max_f16 v20, v20, 0
	v_fma_mixlo_f16 v21, v17, v36, v40 op_sel_hi:[1,0,0]
	v_fma_mixhi_f16 v21, v17, v37, v41 op_sel:[1,0,0] op_sel_hi:[1,0,0]
	v_pk_max_f16 v21, v21, 0
	s_nop 1
	v_cndmask_b32_e32 v14, 0, v18, vcc
	v_cndmask_b32_e32 v15, 0, v19, vcc
	v_lshl_or_b32 v18, v57, 1, v69
	v_ashrrev_i32_e32 v19, 1, v22
	v_mad_u32_u24 v18, v18, 33, v19
	v_lshlrev_b32_e32 v19, 7, v18
	v_xor_b32_e32 v18, v18, v0
	v_lshlrev_b32_e32 v18, 4, v18
	v_and_b32_e32 v18, 0x70, v18
	v_cndmask_b32_e32 v16, 0, v20, vcc
	v_cndmask_b32_e32 v17, 0, v21, vcc
	v_add3_u32 v18, 0, v19, v18
	ds_write_b128 v18, v[14:17]
	v_add_u32_e32 v18, v56, v54
	v_fma_mixlo_f16 v14, v10, v26, v30 op_sel_hi:[1,0,0]
	v_fma_mixhi_f16 v14, v10, v27, v31 op_sel:[1,0,0] op_sel_hi:[1,0,0]
	v_pk_max_f16 v14, v14, 0
	v_add_u32_e32 v10, s27, v18
	v_max_u32_e32 v10, v55, v10
	v_fma_mixlo_f16 v15, v11, v28, v32 op_sel_hi:[1,0,0]
	v_fma_mixhi_f16 v15, v11, v29, v33 op_sel:[1,0,0] op_sel_hi:[1,0,0]
	v_pk_max_f16 v15, v15, 0
	v_cmp_gt_u32_e32 vcc, s10, v10
	v_fma_mixlo_f16 v16, v12, v34, v38 op_sel_hi:[1,0,0]
	v_fma_mixhi_f16 v16, v12, v35, v39 op_sel:[1,0,0] op_sel_hi:[1,0,0]
	v_pk_max_f16 v16, v16, 0
	v_fma_mixlo_f16 v17, v13, v36, v40 op_sel_hi:[1,0,0]
	v_fma_mixhi_f16 v17, v13, v37, v41 op_sel:[1,0,0] op_sel_hi:[1,0,0]
	v_pk_max_f16 v17, v17, 0
	s_nop 1
	v_cndmask_b32_e32 v10, 0, v14, vcc
	v_cndmask_b32_e32 v11, 0, v15, vcc
	v_lshl_or_b32 v14, v53, 1, v69
	v_ashrrev_i32_e32 v15, 1, v18
	v_mad_u32_u24 v14, v14, 33, v15
	v_lshlrev_b32_e32 v15, 7, v14
	v_xor_b32_e32 v14, v14, v0
	v_lshlrev_b32_e32 v14, 4, v14
	v_and_b32_e32 v14, 0x70, v14
	v_cndmask_b32_e32 v12, 0, v16, vcc
	v_cndmask_b32_e32 v13, 0, v17, vcc
	v_add3_u32 v14, 0, v15, v14
	v_cmp_gt_u32_e32 vcc, s6, v0
	ds_write_b128 v14, v[10:13]
	v_fma_mixlo_f16 v10, v6, v26, v30 op_sel_hi:[1,0,0]
	v_fma_mixhi_f16 v10, v6, v27, v31 op_sel:[1,0,0] op_sel_hi:[1,0,0]
	v_pk_max_f16 v10, v10, 0
	v_fma_mixlo_f16 v6, v7, v28, v32 op_sel_hi:[1,0,0]
	v_fma_mixhi_f16 v6, v7, v29, v33 op_sel:[1,0,0] op_sel_hi:[1,0,0]
	v_pk_max_f16 v6, v6, 0
	v_fma_mixlo_f16 v7, v8, v34, v38 op_sel_hi:[1,0,0]
	v_fma_mixhi_f16 v7, v8, v35, v39 op_sel:[1,0,0] op_sel_hi:[1,0,0]
	v_pk_max_f16 v7, v7, 0
	v_fma_mixlo_f16 v8, v9, v36, v40 op_sel_hi:[1,0,0]
	v_fma_mixhi_f16 v8, v9, v37, v41 op_sel:[1,0,0] op_sel_hi:[1,0,0]
	v_pk_max_f16 v8, v8, 0
	s_and_saveexec_b64 s[6:7], vcc
	s_cbranch_execz .LBB3_18
	v_mul_u32_u24_e32 v9, 0x3e1, v52
	v_lshrrev_b32_e32 v9, 16, v9
	s_movk_i32 s11, 0xffbe
	v_mad_i32_i24 v14, v9, s11, v52
	v_add_u32_e32 v11, s25, v9
	v_add_u32_e32 v12, s27, v14
	v_max_u32_e32 v11, v11, v12
	v_cmp_gt_u32_e32 vcc, s10, v11
	s_nop 1
	v_cndmask_b32_e32 v11, 0, v6, vcc
	v_cndmask_b32_e32 v12, 0, v7, vcc
	v_lshl_or_b32 v6, v9, 1, v69
	v_ashrrev_i32_e32 v7, 1, v14
	v_mad_u32_u24 v6, v6, 33, v7
	v_lshlrev_b32_e32 v7, 7, v6
	v_xor_b32_e32 v6, v6, v0
	v_lshlrev_b32_e32 v6, 4, v6
	v_and_b32_e32 v6, 0x70, v6
	v_cndmask_b32_e32 v10, 0, v10, vcc
	v_cndmask_b32_e32 v13, 0, v8, vcc
	v_add3_u32 v6, 0, v7, v6
	ds_write_b128 v6, v[10:13]
